# stack25 = stack23 + out-projection weights touched into the XCD L2 at the start of the phase (one dword per line per thread)
# baseline (speedup 1.0000x reference)
; DEVINL void phase4(const Params& P, unsigned char* smem) {
;     const int t = threadIdx.x, wv = __builtin_amdgcn_readfirstlane(t >> 6);
;     const bf16_t* ATT = (const bf16_t*)(P.ws + WS_ATT); const float* SSQ = (const float*)(P.ws + WS_SSQ);
;     const bf16_t* WrF = (const bf16_t*)(P.ws + WS_WRF);
;     const float* mod = (const float*)(P.ws + WS_MOD);
;     unsigned char* H2 = P.ws + WS_H;
;     bf16_t* X1B = (bf16_t*)(P.ws + WS_X1B); const bf16_t* XB = (const bf16_t*)(P.ws + WS_XB);
;     unsigned* ccnt = (unsigned*)(P.ws + WS_CCNT); int* ctok = (int*)(P.ws + WS_CTOK); f32x2* cw = (f32x2*)(P.ws + WS_CW);
;     float* s_part = (float*)(smem + 131072);
;     float* s_lg = (float*)smem;
;     float* s_t1 = (float*)(smem + 135168); float* s_t2 = s_t1 + 1024; float* s_t3 = s_t2 + 1024;
;     for (int tile = blockIdx.x; tile < NT / 64; tile += gridDim.x) {
;         const int m0 = tile * 64;
;         int lane = t & 63;
;         asm volatile("" : "+v"(lane));
;         const int lr = lane & 15, g = lane >> 4;
;         __syncthreads();
;         {
;             const float* mbt = mod + (m0 >> 13) * 6144;
;             const int c2_ = 2 * t;
;             const f32x2 ga_ = *(const f32x2*)(mbt + 2048 + c2_), gp_ = *(const f32x2*)(P.g_post_mix + c2_), gf_ = *(const f32x2*)(P.g_pre_ffn + c2_), sc_ = *(const f32x2*)(mbt + 4096 + c2_), sh_ = *(const f32x2*)(mbt + 3072 + c2_);
;             *(f32x2*)(s_t1 + c2_) = ga_ * gp_; *(f32x2*)(s_t2 + c2_) = gf_ * (sc_ + 1.f); *(f32x2*)(s_t3 + c2_) = sh_;
;         }
;         {
;             const int row = t >> 3;
;             const float* sp = SSQ + (size_t)(m0 + row) * 16;
;             const f32x4 a = *(const f32x4*)sp, b2 = *(const f32x4*)(sp + 4), c2 = *(const f32x4*)(sp + 8), d2 = *(const f32x4*)(sp + 12);
;             const float rna = rsqrtf((a.x + a.y + a.z + a.w + b2.x + b2.y + b2.z + b2.w) * (1.f / 512.f) + EPS);
;             const float rsw = rsqrtf((c2.x + c2.y + c2.z + c2.w + d2.x + d2.y + d2.z + d2.w) * (1.f / 512.f) + EPS);
;             const bf16_t* src = ATT + (size_t)(m0 + row) * DM;
; #pragma unroll 8
;             for (int i = 0; i < 16; ++i) {
;                 const int c = (t & 7) + 8 * i;
;                 u32x4 v = *(const u32x4*)(src + c * 8);
;                 const float sc = (c < 64) ? rna : rsw;
.LBB0_575:
	s_cmp_lt_i32 s76, 4
	s_cselect_b64 s[4:5], -1, 0
	s_cmp_gt_i32 s77, 3
	s_cselect_b64 s[0:1], -1, 0
	s_and_b64 s[0:1], s[4:5], s[0:1]
	s_andn2_b64 vcc, exec, s[0:1]
	s_cbranch_vccnz .LBB0_641
	s_cmpk_gt_i32 s80, 0xff
	v_readfirstlane_b32 s0, v0
	s_cbranch_scc1 .LBB0_641
	s_add_u32 s16, s34, 0xc300000
	s_addc_u32 s17, s35, 0
	s_add_u32 s2, s34, 0x100000
	s_addc_u32 s3, s35, 0
	s_add_u32 s18, s34, 0x8000
	s_addc_u32 s19, s35, 0
	s_add_u32 s20, s34, 0xe800000
	s_addc_u32 s21, s35, 0
	s_add_u32 s22, s34, 0xf000000
	s_addc_u32 s23, s35, 0
	s_lshr_b32 s33, s0, 6
	s_mov_b32 s25, 0
	s_lshl_b32 s24, s33, 3
	v_lshlrev_b32_e32 v178, 3, v0
	s_add_i32 s1, 0, 0x22000
	s_lshl_b64 s[8:9], s[24:25], 10
	s_lshl_b32 s24, s33, 7
	s_add_i32 s29, 0, 0x21000
	v_add_u32_e32 v189, s1, v178
	s_add_i32 s1, 0, 0x23000
	s_lshl_b64 s[6:7], s[24:25], 1
	s_add_u32 s6, s34, s6
	s_addc_u32 s7, s35, s7
	s_add_u32 s26, s6, 0xc800000
	s_addc_u32 s27, s7, 0
	s_and_b32 s0, s0, 0x3fffffc0
	s_lshl_b32 s0, s0, 2
	v_add_u32_e32 v216, s1, v178
	s_add_i32 s28, s0, 0
	s_mul_i32 s0, s33, 12
	s_mov_b32 s1, s25
	s_add_i32 s28, s28, 0x20000
	s_lshl_b64 s[0:1], s[0:1], 10
	s_add_u32 s0, s34, s0
	s_addc_u32 s1, s35, s1
	s_add_u32 s36, s0, 0x180000
	s_addc_u32 s37, s1, 0
	s_lshl_b32 s10, s33, 9
	v_add_u32_e32 v1, s29, v178
	s_add_i32 s29, s29, s10
	s_add_u32 s38, s6, 0x5b00000
	s_addc_u32 s39, s7, 0
	s_add_i32 s57, 0, 0x24000
	s_add_u32 s40, s96, 0xb8
	s_addc_u32 s41, s97, 0
	v_mov_b32_e32 v179, 0
	s_bitcmp0_b32 s78, 5
	v_lshl_add_u64 v[180:181], s[42:43], 0, v[178:179]
	s_cselect_b64 s[42:43], -1, 0
	s_add_u32 s8, s34, s8
	s_addc_u32 s9, s35, s9
	v_lshl_add_u64 v[182:183], s[44:45], 0, v[178:179]
	s_add_u32 s44, s8, 0x900000
	s_addc_u32 s45, s9, 0
	s_bitcmp0_b32 s78, 6
	s_cselect_b64 s[46:47], -1, 0
	s_bitcmp0_b32 s78, 12
	s_cselect_b64 s[48:49], -1, 0
	s_bitcmp0_b32 s78, 13
	s_cselect_b64 s[50:51], -1, 0
	s_bitcmp0_b32 s78, 0
	v_cmp_gt_u32_e32 vcc, 64, v0
	s_cselect_b64 s[0:1], -1, 0
	s_mov_b64 s[82:83], s[30:31]
	v_and_b32_e32 v218, 7, v0
	s_and_b64 s[30:31], vcc, s[0:1]
	s_mov_b32 s86, s52
	v_lshlrev_b32_e32 v178, 4, v218
	s_add_u32 s52, s8, 0x910000
	s_waitcnt vmcnt(0)
	v_lshl_add_u64 v[4:5], s[34:35], 0, v[178:179]
	s_mov_b64 s[0:1], 0xa300380
	s_addc_u32 s53, s9, 0
	v_lshl_add_u64 v[184:185], v[4:5], 0, s[0:1]
	s_lshr_b32 s0, s80, 3
	s_lshl_b32 s0, s0, 16
	s_add_u32 s0, s0, 0x900000
	s_add_u32 s0, s34, s0
	s_addc_u32 s1, s35, 0
	v_lshlrev_b32_e32 v211, 7, v0
	global_load_dword v211, v211, s[0:1]
	s_add_u32 s0, s34, s24
	s_addc_u32 s1, s35, 0
	v_lshlrev_b32_e32 v2, 1, v0
	v_lshrrev_b32_e32 v217, 3, v0
	v_lshl_add_u32 v221, v0, 4, 0
	s_add_u32 s54, s0, 0x3b00000
	v_lshl_add_u32 v219, v217, 11, 0
	v_bfe_u32 v220, v0, 3, 4
	s_mul_i32 s33, s33, 48
	v_mad_i32_i24 v222, v0, -12, v221
	v_lshl_add_u32 v225, v0, 2, s57
	v_cmp_gt_u32_e64 s[6:7], 48, v0
	s_mov_b32 s63, 0x18000
	v_add_u32_e32 v223, 0x1a000, v221
	v_add_u32_e32 v253, 0x1c000, v221
	v_add_u32_e32 v252, 0x1e000, v221
	s_movk_i32 s66, 0x1000
	s_mov_b64 s[84:85], s[76:77]
	s_addc_u32 s55, s1, 0
	s_add_i32 s67, s10, 0
	v_lshlrev_b32_e32 v186, 2, v2
	v_mov_b32_e32 v187, v179
	s_movk_i32 s68, 0x4000
	s_movk_i32 s69, 0x3000
	s_mov_b32 s56, 0x3b000000
	v_mov_b32_e32 v188, 0x358637bd
	s_mov_b32 s70, 0x800000
	s_mov_b64 s[58:59], 0x400
	s_mov_b64 s[60:61], 0x20000
	s_mov_b32 s71, 0x8000
	s_mov_b32 s62, 0x3a800000
	s_mov_b64 s[64:65], 0x18000
	s_mov_b32 s76, 0x3fb8aa3b
	s_mov_b32 s77, 0xc2ce8ed0
	s_mov_b32 s78, 0x42b17218
	v_mov_b32_e32 v224, 0x7f800000
	s_mov_b32 s79, s80
	s_branch .LBB0_582
